# speedup vs baseline: 1.0018x; 1.0014x over previous
.Lka_done:
	v_max3_f32 v156, v112, v113, v80
	v_max3_f32 v157, v114, v115, v81
	s_nop 0
	v_max3_f32 v156, v156, v82, v83
	v_mfma_f32_32x32x16_bf16 a[16:31], v[176:179], v[144:147], a[16:31]
	v_cvt_pk_bf16_f32 v228, v227, v228
	ds_read_b128 a[224:227], v217 offset:8192
	v_max3_f32 v156, v156, v116, v117
	v_max3_f32 v157, v157, v118, v119
	v_max3_f32 v156, v156, v84, v85
	v_max3_f32 v157, v157, v86, v87
	v_mfma_f32_32x32x16_bf16 a[32:47], v[168:171], v[128:131], a[32:47]
	v_cvt_pk_bf16_f32 v229, v229, v230
	ds_read_b128 a[228:231], v199 offset:8192
	v_max3_f32 v156, v156, v120, v121
	v_max3_f32 v157, v157, v122, v123
	v_max3_f32 v156, v156, v88, v89
	v_max3_f32 v157, v157, v90, v91
	v_mfma_f32_32x32x16_bf16 a[48:63], v[168:171], v[144:147], a[48:63]
	v_cvt_pk_bf16_f32 v230, v231, v232
	ds_read_b128 a[232:235], v198 offset:8192
	v_max3_f32 v156, v156, v124, v125
	v_max3_f32 v157, v157, v126, v127
	v_max3_f32 v156, v156, v92, v93
	v_max3_f32 v157, v157, v94, v95
	v_mfma_f32_32x32x16_bf16 a[64:79], v[160:163], v[128:131], a[64:79]
	v_cvt_pk_bf16_f32 v231, v233, v234
	ds_read_b128 a[236:239], v197 offset:8192
	v_max3_f32 v158, v96, v97, v64
	v_max3_f32 v159, v98, v99, v65
	v_max3_f32 v158, v158, v66, v67
	v_mfma_f32_32x32x16_bf16 a[80:95], v[160:163], v[144:147], a[80:95]
	v_cvt_pk_bf16_f32 v160, v148, v149
	ds_read_b128 a[240:243], v217 offset:8320
	v_max3_f32 v158, v158, v100, v101
	v_max3_f32 v159, v159, v102, v103
	v_max3_f32 v158, v158, v68, v69
	v_max3_f32 v159, v159, v70, v71
	v_mfma_f32_32x32x16_bf16 a[96:111], v[136:139], v[128:131], a[96:111]
	v_cvt_pk_bf16_f32 v161, v150, v151
	ds_read_b128 a[244:247], v199 offset:8320
	v_max3_f32 v128, v158, v104, v105
	v_max3_f32 v129, v159, v106, v107
	v_max3_f32 v128, v128, v72, v73
	v_max3_f32 v129, v129, v74, v75
	v_mfma_f32_32x32x16_bf16 a[112:127], v[136:139], v[144:147], a[112:127]
	v_cvt_pk_bf16_f32 v162, v152, v153
	ds_read_b128 a[248:251], v198 offset:8320
	v_max3_f32 v128, v128, v108, v109
	v_max3_f32 v129, v129, v110, v111
	v_max3_f32 v128, v128, v76, v77
	v_max3_f32 v130, v129, v78, v79
	v_mfma_f32_32x32x16_bf16 a[0:15], v[132:135], v[52:55], a[0:15]
	v_cvt_pk_bf16_f32 v163, v154, v155
	ds_read_b128 a[252:255], v197 offset:8320
	s_cmp_gt_u32 s27, 4
	s_cbranch_scc1 .Lkb2_done
	s_waitcnt lgkmcnt(8)
	v_pk_add_f32 v[200:201], v[248:249], v[200:201]
	v_pk_add_f32 v[202:203], v[250:251], v[202:203]
	v_pk_add_f32 v[204:205], v[252:253], v[204:205]
	v_pk_add_f32 v[206:207], v[254:255], v[206:207]
	v_cvt_pk_bf16_f32 v248, v248, v249
	v_cvt_pk_bf16_f32 v249, v250, v251
	v_cvt_pk_bf16_f32 v250, v252, v253
	v_cvt_pk_bf16_f32 v251, v254, v255
	v_lshrrev_b32_e32 v252, 1, v208
	buffer_store_dwordx4 v[248:251], v252, s[4:7], s56 offen sc1
	s_add_i32 s56, s56, 0x1000
	s_nop 1
	global_load_dwordx4 v[248:251], v208, s[54:55] nt
	global_load_dwordx4 v[252:255], v208, s[54:55] offset:16 nt
	s_add_u32 s54, s54, 0x2000
	s_addc_u32 s55, s55, 0
	s_mov_b32 m0, s84
	s_nop 0
	buffer_load_dwordx4 v208, s[80:83], s86 offen lds
	s_mov_b32 m0, s85
	s_nop 0
	buffer_load_dwordx4 v208, s[80:83], s86 offen offset:16 lds
	s_add_i32 s86, s86, 0x2000

.Lkc_done:
	v_max3_f32 v156, v112, v113, v48
	v_max3_f32 v157, v114, v115, v49
	s_nop 0
	v_max3_f32 v156, v156, v50, v51
	v_mfma_f32_32x32x16_bf16 a[16:31], v[172:175], v[144:147], a[16:31]
	v_cvt_pk_bf16_f32 v228, v227, v228
	ds_read_b128 a[224:227], v218 offset:8192
	v_max3_f32 v156, v156, v116, v117
	v_max3_f32 v157, v157, v118, v119
	v_max3_f32 v156, v156, v52, v53
	v_max3_f32 v157, v157, v54, v55
	v_mfma_f32_32x32x16_bf16 a[32:47], v[164:167], v[128:131], a[32:47]
	v_cvt_pk_bf16_f32 v229, v229, v230
	ds_read_b128 a[228:231], v219 offset:8192
	v_max3_f32 v156, v156, v120, v121
	v_max3_f32 v157, v157, v122, v123
	v_max3_f32 v156, v156, v56, v57
	v_max3_f32 v157, v157, v58, v59
	v_mfma_f32_32x32x16_bf16 a[48:63], v[164:167], v[144:147], a[48:63]
	v_cvt_pk_bf16_f32 v230, v231, v232
	ds_read_b128 a[232:235], v220 offset:8192
	v_max3_f32 v156, v156, v124, v125
	v_max3_f32 v157, v157, v126, v127
	v_max3_f32 v156, v156, v60, v61
	v_max3_f32 v157, v157, v62, v63
	v_mfma_f32_32x32x16_bf16 a[64:79], v[160:163], v[128:131], a[64:79]
	v_cvt_pk_bf16_f32 v231, v233, v234
	ds_read_b128 a[236:239], v221 offset:8192
	v_max3_f32 v158, v96, v97, v32
	v_max3_f32 v159, v98, v99, v33
	v_max3_f32 v158, v158, v34, v35
	v_mfma_f32_32x32x16_bf16 a[80:95], v[160:163], v[144:147], a[80:95]
	v_cvt_pk_bf16_f32 v160, v148, v149
	ds_read_b128 a[240:243], v218 offset:8320
	v_max3_f32 v158, v158, v100, v101
	v_max3_f32 v159, v159, v102, v103
	v_max3_f32 v158, v158, v36, v37
	v_max3_f32 v159, v159, v38, v39
	v_mfma_f32_32x32x16_bf16 a[96:111], v[136:139], v[128:131], a[96:111]
	v_cvt_pk_bf16_f32 v161, v150, v151
	ds_read_b128 a[244:247], v219 offset:8320
	v_max3_f32 v128, v158, v104, v105
	v_max3_f32 v129, v159, v106, v107
	v_max3_f32 v128, v128, v40, v41
	v_max3_f32 v129, v129, v42, v43
	v_mfma_f32_32x32x16_bf16 a[112:127], v[136:139], v[144:147], a[112:127]
	v_cvt_pk_bf16_f32 v162, v152, v153
	ds_read_b128 a[248:251], v220 offset:8320
	v_max3_f32 v128, v128, v108, v109
	v_max3_f32 v129, v129, v110, v111
	v_max3_f32 v128, v128, v44, v45
	v_max3_f32 v130, v129, v46, v47
	v_mfma_f32_32x32x16_bf16 a[0:15], v[132:135], v[84:87], a[0:15]
	v_cvt_pk_bf16_f32 v163, v154, v155
	ds_read_b128 a[252:255], v221 offset:8320
	s_cmp_gt_u32 s27, 4
	s_cbranch_scc1 .Lkd2_done
	s_waitcnt lgkmcnt(8)
	v_pk_add_f32 v[200:201], v[248:249], v[200:201]
	v_pk_add_f32 v[202:203], v[250:251], v[202:203]
	v_pk_add_f32 v[204:205], v[252:253], v[204:205]
	v_pk_add_f32 v[206:207], v[254:255], v[206:207]
	v_cvt_pk_bf16_f32 v248, v248, v249
	v_cvt_pk_bf16_f32 v249, v250, v251
	v_cvt_pk_bf16_f32 v250, v252, v253
	v_cvt_pk_bf16_f32 v251, v254, v255
	v_lshrrev_b32_e32 v252, 1, v208
	buffer_store_dwordx4 v[248:251], v252, s[4:7], s56 offen sc1
	s_add_i32 s56, s56, 0x1000
	s_nop 1
	global_load_dwordx4 v[248:251], v208, s[54:55] nt
	global_load_dwordx4 v[252:255], v208, s[54:55] offset:16 nt
	s_add_u32 s54, s54, 0x2000
	s_addc_u32 s55, s55, 0
	s_cmp_gt_u32 s27, 2
	s_cbranch_scc1 .Lkd2_done
	s_mov_b32 m0, s84
	s_nop 0
	buffer_load_dwordx4 v208, s[80:83], s86 offen lds
	s_mov_b32 m0, s85
	s_nop 0
	buffer_load_dwordx4 v208, s[80:83], s86 offen offset:16 lds
	s_add_i32 s86, s86, 0x2000
